# v40
# baseline (speedup 1.0000x reference)
.Lprio_half:
	ds_read_b128 v[0:3], v72 offset:12288
	ds_read_b128 v[4:7], v71 offset:42752
	ds_read_b128 v[8:11], v72 offset:13312
	ds_read_b128 v[12:15], v72 offset:14336
	ds_read_b128 v[34:37], v72 offset:15360
	ds_read_b128 v[44:47], v71 offset:42816
	v_cvt_pk_f16_f32 v30, v52, v53
	v_cvt_pk_f16_f32 v26, v26, v27
	v_cvt_pk_f16_f32 v31, v54, v55
	s_waitcnt lgkmcnt(4)
	v_mfma_f32_16x16x32_f16 v[48:51], v[0:3], v[22:25], v[4:7]
	v_cvt_pk_f16_f32 v32, v56, v57
	v_cvt_pk_f16_f32 v33, v58, v59
	v_cvt_pk_f16_f32 v27, v28, v29
	v_mfma_f32_16x16x32_f16 v[0:3], v[0:3], v[18:21], v[4:7]
	v_cvt_pk_f16_f32 v28, v16, v17
	s_add_i32 s11, s9, s12
	s_waitcnt lgkmcnt(3)
	v_mfma_f32_16x16x32_f16 v[48:51], v[8:11], v[30:33], v[48:51]
	s_cmp_lt_i32 s11, 0x8000
	v_cvt_pk_f16_f32 v29, v60, v61
	s_cselect_b32 s10, s11, s10
	s_ashr_i32 s11, s10, 31
	v_mfma_f32_16x16x32_f16 v[52:55], v[8:11], v[26:29], v[0:3]
	ds_read_b128 v[4:7], v72 offset:17408
	ds_read_b128 v[8:11], v71 offset:42880
	s_lshl_b64 s[10:11], s[10:11], 12
	s_add_u32 s10, s10, s36
	s_addc_u32 s11, s11, s37
	ds_read_b128 v[0:3], v72 offset:16384
	s_waitcnt lgkmcnt(3)
	v_exp_f32_e32 v106, v48
	v_mfma_f32_16x16x32_f16 v[56:59], v[12:15], v[22:25], v[44:47]
	v_exp_f32_e32 v107, v49
	v_exp_f32_e32 v110, v50
	v_mfma_f32_16x16x32_f16 v[12:15], v[12:15], v[18:21], v[44:47]
	v_exp_f32_e32 v111, v51
	v_exp_f32_e32 v114, v52
	v_mfma_f32_16x16x32_f16 v[44:47], v[34:37], v[30:33], v[56:59]
	v_exp_f32_e32 v115, v53
	v_mfma_f32_16x16x32_f16 v[56:59], v[34:37], v[26:29], v[12:15]
	ds_read_b128 v[34:37], v72 offset:19456
	ds_read_b128 v[60:63], v71 offset:42944
	s_nop 4
	v_exp_f32_e64 v108, v44 clamp
	ds_read_b128 v[12:15], v72 offset:18432
	s_waitcnt lgkmcnt(3)
	v_mfma_f32_16x16x32_f16 v[64:67], v[0:3], v[22:25], v[8:11]
	v_exp_f32_e64 v109, v45 clamp
	v_mfma_f32_16x16x32_f16 v[0:3], v[0:3], v[18:21], v[8:11]
	v_exp_f32_e64 v116, v56 clamp
	v_mfma_f32_16x16x32_f16 v[64:67], v[4:7], v[30:33], v[64:67]
	v_exp_f32_e64 v59, v59 clamp
	v_mfma_f32_16x16x32_f16 v[74:77], v[4:7], v[26:29], v[0:3]
	ds_read_b128 v[78:81], v72 offset:20480
	ds_read_b128 v[82:85], v72 offset:21504
	ds_read_b128 v[86:89], v71 offset:43008
	s_waitcnt lgkmcnt(3)
	v_exp_f32_e64 v58, v58 clamp
	v_mfma_f32_16x16x32_f16 v[6:9], v[12:15], v[22:25], v[60:63]
	v_exp_f32_e64 v117, v57 clamp
	v_mfma_f32_16x16x32_f16 v[60:63], v[12:15], v[18:21], v[60:63]
	global_load_dwordx4 v[10:13], v39, s[10:11] offset:16
	global_load_dwordx4 v[14:17], v39, s[10:11]
	global_load_dwordx4 v[2:5], v39, s[10:11] offset:2064
	v_exp_f32_e64 v113, v47 clamp
	v_mfma_f32_16x16x32_f16 v[90:93], v[34:37], v[30:33], v[6:9]
	v_exp_f32_e64 v112, v46 clamp
	v_mfma_f32_16x16x32_f16 v[60:63], v[34:37], v[26:29], v[60:63]
	s_nop 1
	global_load_dwordx4 v[6:9], v39, s[10:11] offset:2048
	ds_read_b128 v[94:97], v72 offset:22528
	ds_read_b128 v[98:101], v72 offset:23552
	ds_read_b128 v[102:105], v71 offset:43072
	s_waitcnt lgkmcnt(3)
	v_exp_f32_e32 v0, v64
	v_mfma_f32_16x16x32_f16 v[44:47], v[78:81], v[22:25], v[86:89]
	v_exp_f32_e32 v1, v65
	v_exp_f32_e32 v34, v66
	v_mfma_f32_16x16x32_f16 v[48:51], v[78:81], v[18:21], v[86:89]
	v_exp_f32_e32 v35, v67
	v_exp_f32_e32 v36, v74
	v_exp_f32_e32 v37, v75
	v_mfma_f32_16x16x32_f16 v[64:67], v[82:85], v[30:33], v[44:47]
	v_exp_f32_e32 v74, v54
	v_exp_f32_e32 v75, v55
	v_exp_f32_e32 v78, v92
	v_mfma_f32_16x16x32_f16 v[50:53], v[82:85], v[26:29], v[48:51]
	v_exp_f32_e32 v44, v76
	v_exp_f32_e32 v45, v77
	v_exp_f32_e32 v76, v90
	s_waitcnt lgkmcnt(0)
	v_mfma_f32_16x16x32_f16 v[46:49], v[94:97], v[22:25], v[102:105]
	v_exp_f32_e32 v77, v91
	v_exp_f32_e64 v64, v64 clamp
	v_exp_f32_e64 v65, v65 clamp
	v_mfma_f32_16x16x32_f16 v[54:57], v[94:97], v[18:21], v[102:105]
	v_exp_f32_e32 v79, v93
	v_exp_f32_e64 v66, v66 clamp
	v_exp_f32_e64 v67, v67 clamp
	v_mfma_f32_16x16x32_f16 v[46:49], v[98:101], v[30:33], v[46:49]
	v_exp_f32_e32 v60, v60
	v_exp_f32_e32 v61, v61
	v_exp_f32_e64 v50, v50 clamp
	v_mfma_f32_16x16x32_f16 v[54:57], v[98:101], v[26:29], v[54:57]
	v_exp_f32_e64 v51, v51 clamp
	s_nop 2
	v_exp_f32_e32 v46, v46
	v_exp_f32_e32 v47, v47
	v_exp_f32_e32 v48, v48
	v_exp_f32_e32 v49, v49
	v_exp_f32_e32 v54, v54
	v_exp_f32_e32 v55, v55
	v_exp_f32_e32 v62, v62
	v_exp_f32_e32 v63, v63
	v_exp_f32_e64 v52, v52 clamp
	v_exp_f32_e64 v53, v53 clamp
	v_exp_f32_e32 v56, v56
	v_exp_f32_e32 v57, v57
	v_pk_fma_f32 v[80:81], v[108:109], s[2:3], 1.0 op_sel_hi:[1,0,0]
	v_pk_fma_f32 v[82:83], v[112:113], s[2:3], 1.0 op_sel_hi:[1,0,0]
	v_pk_fma_f32 v[84:85], v[116:117], s[2:3], 1.0 op_sel_hi:[1,0,0]
	v_pk_fma_f32 v[58:59], v[58:59], s[2:3], 1.0 op_sel_hi:[1,0,0]
	v_pk_fma_f32 v[64:65], v[64:65], s[2:3], 1.0 op_sel_hi:[1,0,0]
	v_pk_fma_f32 v[66:67], v[66:67], s[2:3], 1.0 op_sel_hi:[1,0,0]
	v_pk_fma_f32 v[50:51], v[50:51], s[2:3], 1.0 op_sel_hi:[1,0,0]
	v_pk_fma_f32 v[52:53], v[52:53], s[2:3], 1.0 op_sel_hi:[1,0,0]
	v_pk_fma_f32 v[86:87], v[106:107], v[80:81], v[80:81]
	v_pk_fma_f32 v[88:89], v[110:111], v[82:83], v[82:83]
	v_pk_fma_f32 v[90:91], v[114:115], v[84:85], v[84:85]
	v_pk_fma_f32 v[74:75], v[74:75], v[58:59], v[58:59]
	v_pk_fma_f32 v[76:77], v[76:77], v[64:65], v[64:65]
	v_pk_fma_f32 v[78:79], v[78:79], v[66:67], v[66:67]
	v_pk_fma_f32 v[60:61], v[60:61], v[50:51], v[50:51]
	v_pk_fma_f32 v[62:63], v[62:63], v[52:53], v[52:53]
	v_pk_fma_f32 v[80:81], v[80:81], s[6:7], v[40:41] op_sel_hi:[1,0,0] neg_lo:[1,0,0] neg_hi:[1,0,0]
	v_pk_fma_f32 v[82:83], v[82:83], s[6:7], v[40:41] op_sel_hi:[1,0,0] neg_lo:[1,0,0] neg_hi:[1,0,0]
	v_pk_fma_f32 v[84:85], v[84:85], s[6:7], v[40:41] op_sel_hi:[1,0,0] neg_lo:[1,0,0] neg_hi:[1,0,0]
	v_pk_fma_f32 v[58:59], v[58:59], s[6:7], v[40:41] op_sel_hi:[1,0,0] neg_lo:[1,0,0] neg_hi:[1,0,0]
	v_pk_fma_f32 v[64:65], v[64:65], s[6:7], v[40:41] op_sel_hi:[1,0,0] neg_lo:[1,0,0] neg_hi:[1,0,0]
	v_pk_fma_f32 v[66:67], v[66:67], s[6:7], v[40:41] op_sel_hi:[1,0,0] neg_lo:[1,0,0] neg_hi:[1,0,0]
	v_pk_fma_f32 v[50:51], v[50:51], s[6:7], v[40:41] op_sel_hi:[1,0,0] neg_lo:[1,0,0] neg_hi:[1,0,0]
	v_pk_fma_f32 v[52:53], v[52:53], s[6:7], v[40:41] op_sel_hi:[1,0,0] neg_lo:[1,0,0] neg_hi:[1,0,0]
	v_pk_fma_f32 v[86:87], v[0:1], v[86:87], v[86:87]
	v_pk_fma_f32 v[88:89], v[34:35], v[88:89], v[88:89]
	v_pk_fma_f32 v[90:91], v[36:37], v[90:91], v[90:91]
	v_pk_fma_f32 v[74:75], v[44:45], v[74:75], v[74:75]
	v_pk_fma_f32 v[76:77], v[46:47], v[76:77], v[76:77]
	v_pk_fma_f32 v[78:79], v[48:49], v[78:79], v[78:79]
	v_pk_fma_f32 v[60:61], v[54:55], v[60:61], v[60:61]
	v_pk_fma_f32 v[62:63], v[56:57], v[62:63], v[62:63]
	v_rcp_f32_e64 v86, v86 clamp
	v_rcp_f32_e64 v87, v87 clamp
	v_rcp_f32_e64 v88, v88 clamp
	v_rcp_f32_e64 v89, v89 clamp
	v_rcp_f32_e64 v90, v90 clamp
	v_rcp_f32_e64 v91, v91 clamp
	v_rcp_f32_e64 v74, v74 clamp
	v_rcp_f32_e64 v75, v75 clamp
	v_rcp_f32_e64 v76, v76 clamp
	v_rcp_f32_e64 v77, v77 clamp
	v_rcp_f32_e64 v78, v78 clamp
	v_rcp_f32_e64 v79, v79 clamp
	v_rcp_f32_e64 v60, v60 clamp
	v_rcp_f32_e64 v61, v61 clamp
	v_rcp_f32_e64 v62, v62 clamp
	v_rcp_f32_e64 v63, v63 clamp
	v_pk_mul_f32 v[80:81], v[80:81], v[86:87]
	v_pk_mul_f32 v[82:83], v[82:83], v[88:89]
	v_pk_mul_f32 v[84:85], v[84:85], v[90:91]
	v_pk_mul_f32 v[58:59], v[58:59], v[74:75]
	v_pk_mul_f32 v[64:65], v[64:65], v[76:77]
	v_pk_mul_f32 v[66:67], v[66:67], v[78:79]
	v_pk_mul_f32 v[50:51], v[50:51], v[60:61]
	v_pk_mul_f32 v[60:61], v[52:53], v[62:63]
	v_pk_fma_f32 v[0:1], v[0:1], v[80:81], v[80:81]
	v_pk_fma_f32 v[34:35], v[34:35], v[82:83], v[82:83]
	v_pk_fma_f32 v[36:37], v[36:37], v[84:85], v[84:85]
	v_pk_fma_f32 v[44:45], v[44:45], v[58:59], v[58:59]
	v_pk_fma_f32 v[46:47], v[46:47], v[64:65], v[64:65]
	v_pk_fma_f32 v[48:49], v[48:49], v[66:67], v[66:67]
	v_pk_fma_f32 v[52:53], v[54:55], v[50:51], v[50:51]
	v_pk_fma_f32 v[54:55], v[56:57], v[60:61], v[60:61]
	s_nop 0
	v_pk_fma_f32 v[0:1], v[0:1], v[0:1], s[4:5] neg_lo:[1,0,0] neg_hi:[1,0,0] clamp
	v_pk_fma_f32 v[34:35], v[34:35], v[34:35], s[4:5] neg_lo:[1,0,0] neg_hi:[1,0,0] clamp
	v_pk_fma_f32 v[36:37], v[36:37], v[36:37], s[4:5] neg_lo:[1,0,0] neg_hi:[1,0,0] clamp
	v_pk_fma_f32 v[44:45], v[44:45], v[44:45], s[4:5] neg_lo:[1,0,0] neg_hi:[1,0,0] clamp
	v_pk_fma_f32 v[46:47], v[46:47], v[46:47], s[4:5] neg_lo:[1,0,0] neg_hi:[1,0,0] clamp
	v_pk_fma_f32 v[48:49], v[48:49], v[48:49], s[4:5] neg_lo:[1,0,0] neg_hi:[1,0,0] clamp
	v_pk_fma_f32 v[52:53], v[52:53], v[52:53], s[4:5] neg_lo:[1,0,0] neg_hi:[1,0,0] clamp
	s_nop 0
	v_pk_fma_f32 v[54:55], v[54:55], v[54:55], s[4:5] neg_lo:[1,0,0] neg_hi:[1,0,0] clamp
	s_nop 0
	v_pk_fma_f32 v[0:1], v[0:1], v[0:1], s[8:9] op_sel_hi:[1,1,0]
	v_pk_fma_f32 v[56:57], v[34:35], v[34:35], s[8:9] op_sel_hi:[1,1,0]
	v_pk_fma_f32 v[36:37], v[36:37], v[36:37], s[8:9] op_sel_hi:[1,1,0]
	v_pk_fma_f32 v[44:45], v[44:45], v[44:45], s[8:9] op_sel_hi:[1,1,0]
	v_pk_fma_f32 v[46:47], v[46:47], v[46:47], s[8:9] op_sel_hi:[1,1,0]
	v_pk_fma_f32 v[48:49], v[48:49], v[48:49], s[8:9] op_sel_hi:[1,1,0]
	v_pk_fma_f32 v[62:63], v[52:53], v[52:53], s[8:9] op_sel_hi:[1,1,0]
	v_pk_fma_f32 v[74:75], v[54:55], v[54:55], s[8:9] op_sel_hi:[1,1,0]
	v_pk_mul_f32 v[34:35], v[80:81], v[0:1]
	v_pk_mul_f32 v[56:57], v[82:83], v[56:57]
	v_pk_mul_f32 v[36:37], v[84:85], v[36:37]
	v_pk_mul_f32 v[52:53], v[58:59], v[44:45]
	v_pk_mul_f32 v[54:55], v[64:65], v[46:47]
	v_pk_mul_f32 v[0:1], v[66:67], v[48:49]
	v_pk_mul_f32 v[46:47], v[62:63], v[50:51]
	v_pk_mul_f32 v[44:45], v[60:61], v[74:75]
	ds_read_b128 v[48:51], v72 offset:24576
	ds_read_b128 v[58:61], v71 offset:43136
	ds_read_b128 v[62:65], v72 offset:25600
	ds_read_b128 v[74:77], v72 offset:26624
	ds_read_b128 v[78:81], v72 offset:27648
	ds_read_b128 v[82:85], v71 offset:43200
	v_cvt_pk_f16_f32 v34, v34, v35
	s_waitcnt lgkmcnt(4)
	v_mfma_f32_16x16x32_f16 v[86:89], v[48:51], v[22:25], v[58:61]
	v_cvt_pk_f16_f32 v35, v56, v57
	v_mfma_f32_16x16x32_f16 v[48:51], v[48:51], v[18:21], v[58:61]
	s_waitcnt lgkmcnt(3)
	v_mfma_f32_16x16x32_f16 v[58:61], v[62:65], v[30:33], v[86:89]
	v_mfma_f32_16x16x32_f16 v[86:89], v[62:65], v[26:29], v[48:51]
	ds_read_b128 v[62:65], v72 offset:29696
	ds_read_b128 v[90:93], v71 offset:43264
	s_nop 2
	ds_read_b128 v[48:51], v72 offset:28672
	s_waitcnt lgkmcnt(3)
	v_mfma_f32_16x16x32_f16 v[94:97], v[74:77], v[22:25], v[82:85]
	v_exp_f32_e32 v120, v86
	v_mfma_f32_16x16x32_f16 v[74:77], v[74:77], v[18:21], v[82:85]
	v_exp_f32_e32 v123, v89
	v_mfma_f32_16x16x32_f16 v[82:85], v[78:81], v[30:33], v[94:97]
	v_exp_f32_e32 v122, v88
	v_mfma_f32_16x16x32_f16 v[74:77], v[78:81], v[26:29], v[74:77]
	ds_read_b128 v[78:81], v72 offset:30720
	s_nop 0
	ds_read_b128 v[94:97], v72 offset:31744
	ds_read_b128 v[98:101], v71 offset:43328
	s_waitcnt lgkmcnt(3)
	v_exp_f32_e32 v121, v87
	v_mfma_f32_16x16x32_f16 v[102:105], v[48:51], v[22:25], v[90:93]
	s_nop 0
	v_exp_f32_e64 v66, v82 clamp
	v_exp_f32_e64 v67, v83 clamp
	v_exp_f32_e64 v118, v84 clamp
	v_mfma_f32_16x16x32_f16 v[48:51], v[48:51], v[18:21], v[90:93]
	v_exp_f32_e64 v119, v85 clamp
	v_exp_f32_e64 v124, v74 clamp
	v_exp_f32_e64 v125, v75 clamp
	v_mfma_f32_16x16x32_f16 v[90:93], v[62:65], v[30:33], v[102:105]
	v_exp_f32_e64 v126, v76 clamp
	v_exp_f32_e64 v127, v77 clamp
	v_mfma_f32_16x16x32_f16 v[102:105], v[62:65], v[26:29], v[48:51]
	ds_read_b128 v[106:109], v72 offset:32768
	ds_read_b128 v[110:113], v72 offset:33792
	v_exp_f32_e32 v62, v58
	v_exp_f32_e32 v63, v59
	v_exp_f32_e32 v64, v60
	v_exp_f32_e32 v65, v61
	ds_read_b128 v[114:117], v71 offset:43392
	s_waitcnt lgkmcnt(3)
	v_mfma_f32_16x16x32_f16 v[58:61], v[78:81], v[22:25], v[98:101]
	v_exp_f32_e32 v48, v90
	v_exp_f32_e32 v49, v91
	v_mfma_f32_16x16x32_f16 v[78:81], v[78:81], v[18:21], v[98:101]
	v_exp_f32_e32 v51, v93
	v_mfma_f32_16x16x32_f16 v[82:85], v[94:97], v[30:33], v[58:61]
	v_exp_f32_e32 v50, v92
	v_mfma_f32_16x16x32_f16 v[78:81], v[94:97], v[26:29], v[78:81]
	ds_read_b128 v[86:89], v72 offset:34816
	ds_read_b128 v[90:93], v72 offset:35840
	ds_read_b128 v[94:97], v71 offset:43456
	s_waitcnt lgkmcnt(3)
	v_exp_f32_e32 v58, v102
	v_mfma_f32_16x16x32_f16 v[74:77], v[106:109], v[22:25], v[114:117]
	v_exp_f32_e32 v59, v103
	v_exp_f32_e32 v60, v104
	v_mfma_f32_16x16x32_f16 v[98:101], v[106:109], v[18:21], v[114:117]
	v_exp_f32_e32 v61, v105
	v_exp_f32_e32 v102, v82
	v_exp_f32_e32 v103, v83
	v_exp_f32_e32 v104, v84
	v_mfma_f32_16x16x32_f16 v[74:77], v[110:113], v[30:33], v[74:77]
	v_exp_f32_e32 v105, v85
	v_mfma_f32_16x16x32_f16 v[82:85], v[110:113], v[26:29], v[98:101]
	s_waitcnt lgkmcnt(0)
	v_mfma_f32_16x16x32_f16 v[18:21], v[86:89], v[18:21], v[94:97]
	s_nop 4
	v_exp_f32_e64 v106, v74 clamp
	v_exp_f32_e64 v107, v75 clamp
	v_exp_f32_e64 v108, v76 clamp
	v_exp_f32_e64 v109, v77 clamp
	v_mfma_f32_16x16x32_f16 v[74:77], v[86:89], v[22:25], v[94:97]
	v_cvt_pk_f16_f32 v22, v36, v37
	v_cvt_pk_f16_f32 v23, v52, v53
	v_cvt_pk_f16_f32 v36, v54, v55
	v_mfma_f32_16x16x32_f16 v[18:21], v[90:93], v[26:29], v[18:21]
	v_exp_f32_e32 v52, v78
	v_exp_f32_e32 v53, v79
	v_exp_f32_e64 v54, v82 clamp
	v_mfma_f32_16x16x32_f16 v[30:33], v[90:93], v[30:33], v[74:77]
	v_exp_f32_e64 v55, v83 clamp
	s_nop 2
	v_exp_f32_e32 v18, v18
	v_exp_f32_e32 v19, v19
	v_exp_f32_e32 v26, v80
	v_exp_f32_e32 v27, v81
	v_exp_f32_e32 v30, v30
	v_exp_f32_e32 v31, v31
	v_exp_f32_e32 v32, v32
	v_exp_f32_e32 v33, v33
	v_exp_f32_e64 v28, v84 clamp
	v_exp_f32_e64 v29, v85 clamp
	v_exp_f32_e32 v20, v20
	v_cvt_pk_f16_f32 v24, v46, v47
	v_cvt_pk_f16_f32 v37, v0, v1
	v_cvt_pk_f16_f32 v25, v44, v45
	v_exp_f32_e32 v21, v21
	v_pk_fma_f32 v[0:1], v[66:67], s[2:3], 1.0 op_sel_hi:[1,0,0]
	v_pk_fma_f32 v[44:45], v[118:119], s[2:3], 1.0 op_sel_hi:[1,0,0]
	v_pk_fma_f32 v[46:47], v[124:125], s[2:3], 1.0 op_sel_hi:[1,0,0]
	v_pk_fma_f32 v[56:57], v[126:127], s[2:3], 1.0 op_sel_hi:[1,0,0]
	v_pk_fma_f32 v[66:67], v[106:107], s[2:3], 1.0 op_sel_hi:[1,0,0]
	v_pk_fma_f32 v[74:75], v[108:109], s[2:3], 1.0 op_sel_hi:[1,0,0]
	v_pk_fma_f32 v[54:55], v[54:55], s[2:3], 1.0 op_sel_hi:[1,0,0]
	v_pk_fma_f32 v[28:29], v[28:29], s[2:3], 1.0 op_sel_hi:[1,0,0]
	v_pk_fma_f32 v[62:63], v[62:63], v[0:1], v[0:1]
	v_pk_fma_f32 v[64:65], v[64:65], v[44:45], v[44:45]
	v_pk_fma_f32 v[76:77], v[120:121], v[46:47], v[46:47]
	v_pk_fma_f32 v[78:79], v[122:123], v[56:57], v[56:57]
	v_pk_fma_f32 v[80:81], v[102:103], v[66:67], v[66:67]
	v_pk_fma_f32 v[82:83], v[104:105], v[74:75], v[74:75]
	v_pk_fma_f32 v[52:53], v[52:53], v[54:55], v[54:55]
	v_pk_fma_f32 v[26:27], v[26:27], v[28:29], v[28:29]
	v_pk_fma_f32 v[0:1], v[0:1], s[6:7], v[40:41] op_sel_hi:[1,0,0] neg_lo:[1,0,0] neg_hi:[1,0,0]
	v_pk_fma_f32 v[44:45], v[44:45], s[6:7], v[40:41] op_sel_hi:[1,0,0] neg_lo:[1,0,0] neg_hi:[1,0,0]
	v_pk_fma_f32 v[46:47], v[46:47], s[6:7], v[40:41] op_sel_hi:[1,0,0] neg_lo:[1,0,0] neg_hi:[1,0,0]
	v_pk_fma_f32 v[56:57], v[56:57], s[6:7], v[40:41] op_sel_hi:[1,0,0] neg_lo:[1,0,0] neg_hi:[1,0,0]
	v_pk_fma_f32 v[66:67], v[66:67], s[6:7], v[40:41] op_sel_hi:[1,0,0] neg_lo:[1,0,0] neg_hi:[1,0,0]
	v_pk_fma_f32 v[74:75], v[74:75], s[6:7], v[40:41] op_sel_hi:[1,0,0] neg_lo:[1,0,0] neg_hi:[1,0,0]
	v_pk_fma_f32 v[54:55], v[54:55], s[6:7], v[40:41] op_sel_hi:[1,0,0] neg_lo:[1,0,0] neg_hi:[1,0,0]
	v_pk_fma_f32 v[28:29], v[28:29], s[6:7], v[40:41] op_sel_hi:[1,0,0] neg_lo:[1,0,0] neg_hi:[1,0,0]
	v_pk_fma_f32 v[62:63], v[48:49], v[62:63], v[62:63]
	v_pk_fma_f32 v[64:65], v[50:51], v[64:65], v[64:65]
	v_pk_fma_f32 v[76:77], v[58:59], v[76:77], v[76:77]
	v_pk_fma_f32 v[78:79], v[60:61], v[78:79], v[78:79]
	v_pk_fma_f32 v[80:81], v[30:31], v[80:81], v[80:81]
	v_pk_fma_f32 v[82:83], v[32:33], v[82:83], v[82:83]
	v_pk_fma_f32 v[52:53], v[18:19], v[52:53], v[52:53]
	v_pk_fma_f32 v[26:27], v[20:21], v[26:27], v[26:27]
	v_rcp_f32_e64 v62, v62 clamp
	v_rcp_f32_e64 v63, v63 clamp
	v_rcp_f32_e64 v64, v64 clamp
	v_rcp_f32_e64 v65, v65 clamp
	v_rcp_f32_e64 v76, v76 clamp
	v_rcp_f32_e64 v77, v77 clamp
	v_rcp_f32_e64 v78, v78 clamp
	v_rcp_f32_e64 v79, v79 clamp
	v_rcp_f32_e64 v80, v80 clamp
	v_rcp_f32_e64 v81, v81 clamp
	v_rcp_f32_e64 v82, v82 clamp
	v_rcp_f32_e64 v83, v83 clamp
	v_rcp_f32_e64 v52, v52 clamp
	v_rcp_f32_e64 v53, v53 clamp
	v_rcp_f32_e64 v26, v26 clamp
	v_rcp_f32_e64 v27, v27 clamp
	v_pk_mul_f32 v[52:53], v[54:55], v[52:53]
	v_pk_mul_f32 v[0:1], v[0:1], v[62:63]
	v_pk_mul_f32 v[44:45], v[44:45], v[64:65]
	v_pk_mul_f32 v[46:47], v[46:47], v[76:77]
	v_pk_mul_f32 v[56:57], v[56:57], v[78:79]
	v_pk_mul_f32 v[62:63], v[66:67], v[80:81]
	v_pk_mul_f32 v[64:65], v[74:75], v[82:83]
	v_pk_mul_f32 v[26:27], v[28:29], v[26:27]
	v_pk_fma_f32 v[18:19], v[18:19], v[52:53], v[52:53]
	v_pk_fma_f32 v[28:29], v[48:49], v[0:1], v[0:1]
	v_pk_fma_f32 v[48:49], v[50:51], v[44:45], v[44:45]
	v_pk_fma_f32 v[50:51], v[58:59], v[46:47], v[46:47]
	v_pk_fma_f32 v[54:55], v[60:61], v[56:57], v[56:57]
	v_pk_fma_f32 v[30:31], v[30:31], v[62:63], v[62:63]
	v_pk_fma_f32 v[32:33], v[32:33], v[64:65], v[64:65]
	v_pk_fma_f32 v[20:21], v[20:21], v[26:27], v[26:27]
	s_nop 0
	v_pk_fma_f32 v[28:29], v[28:29], v[28:29], s[4:5] neg_lo:[1,0,0] neg_hi:[1,0,0] clamp
	v_pk_fma_f32 v[48:49], v[48:49], v[48:49], s[4:5] neg_lo:[1,0,0] neg_hi:[1,0,0] clamp
	v_pk_fma_f32 v[50:51], v[50:51], v[50:51], s[4:5] neg_lo:[1,0,0] neg_hi:[1,0,0] clamp
	v_pk_fma_f32 v[54:55], v[54:55], v[54:55], s[4:5] neg_lo:[1,0,0] neg_hi:[1,0,0] clamp
	v_pk_fma_f32 v[30:31], v[30:31], v[30:31], s[4:5] neg_lo:[1,0,0] neg_hi:[1,0,0] clamp
	v_pk_fma_f32 v[32:33], v[32:33], v[32:33], s[4:5] neg_lo:[1,0,0] neg_hi:[1,0,0] clamp
	v_pk_fma_f32 v[18:19], v[18:19], v[18:19], s[4:5] neg_lo:[1,0,0] neg_hi:[1,0,0] clamp
	s_nop 0
	v_pk_fma_f32 v[20:21], v[20:21], v[20:21], s[4:5] neg_lo:[1,0,0] neg_hi:[1,0,0] clamp
	s_nop 0
	v_pk_fma_f32 v[28:29], v[28:29], v[28:29], s[8:9] op_sel_hi:[1,1,0]
	v_pk_fma_f32 v[48:49], v[48:49], v[48:49], s[8:9] op_sel_hi:[1,1,0]
	v_pk_fma_f32 v[50:51], v[50:51], v[50:51], s[8:9] op_sel_hi:[1,1,0]
	v_pk_fma_f32 v[54:55], v[54:55], v[54:55], s[8:9] op_sel_hi:[1,1,0]
	v_pk_fma_f32 v[30:31], v[30:31], v[30:31], s[8:9] op_sel_hi:[1,1,0]
	v_pk_fma_f32 v[32:33], v[32:33], v[32:33], s[8:9] op_sel_hi:[1,1,0]
	v_pk_fma_f32 v[18:19], v[18:19], v[18:19], s[8:9] op_sel_hi:[1,1,0]
	v_pk_fma_f32 v[20:21], v[20:21], v[20:21], s[8:9] op_sel_hi:[1,1,0]
	v_pk_mul_f32 v[0:1], v[0:1], v[28:29]
	v_pk_mul_f32 v[58:59], v[44:45], v[48:49]
	v_pk_mul_f32 v[60:61], v[46:47], v[50:51]
	v_pk_mul_f32 v[54:55], v[56:57], v[54:55]
	v_pk_mul_f32 v[62:63], v[62:63], v[30:31]
	v_pk_mul_f32 v[64:65], v[64:65], v[32:33]
	v_pk_mul_f32 v[66:67], v[18:19], v[52:53]
	v_pk_mul_f32 v[74:75], v[26:27], v[20:21]
	ds_read_b128 v[18:21], v72 offset:36864
	ds_read_b128 v[30:33], v72 offset:37888
	ds_read_b128 v[26:29], v71 offset:43520
	v_cvt_pk_f16_f32 v56, v60, v61
	v_cvt_pk_f16_f32 v57, v54, v55
	v_cvt_pk_f16_f32 v54, v62, v63
	ds_read_b128 v[60:63], v71 offset:43584
	v_cvt_pk_f16_f32 v52, v0, v1
	v_cvt_pk_f16_f32 v53, v58, v59
	s_waitcnt lgkmcnt(1)
	v_mfma_f32_16x16x32_f16 v[48:51], v[18:21], v[34:37], v[26:29]
	v_cvt_pk_f16_f32 v55, v64, v65
	v_cvt_pk_f16_f32 v58, v66, v67
	v_mfma_f32_16x16x32_f16 v[18:21], v[18:21], v[22:25], v[26:29]
	ds_read_b128 v[44:47], v72 offset:40960
	s_add_i32 s12, s12, s3
	s_add_i32 s10, s20, s12
	v_cvt_pk_f16_f32 v59, v74, v75
	v_mfma_f32_16x16x32_f16 v[26:29], v[30:33], v[52:55], v[48:51]
	s_cmp_lt_i32 s10, 0x8000
	v_add_u32_e32 v38, s7, v38
	s_nop 0
	ds_read_b128 v[48:51], v72 offset:38912
	v_mfma_f32_16x16x32_f16 v[18:21], v[30:33], v[56:59], v[18:21]
	ds_read_b128 v[30:33], v72 offset:39936
	s_nop 1
	v_cvt_pk_f16_f32 v1, v28, v29
	v_cvt_pk_f16_f32 v0, v26, v27
	s_waitcnt lgkmcnt(1)
	v_mfma_f32_16x16x32_f16 v[34:37], v[48:51], v[34:37], v[60:63]
	v_pk_max_f16 v27, v1, 0
	v_cvt_pk_f16_f32 v1, v20, v21
	v_pk_max_f16 v26, v0, 0
	v_mfma_f32_16x16x32_f16 v[20:23], v[48:51], v[22:25], v[60:63]
	v_cvt_pk_f16_f32 v0, v18, v19
	v_pk_max_f16 v18, v0, 0
	s_waitcnt lgkmcnt(0)
	v_mfma_f32_16x16x32_f16 v[34:37], v[30:33], v[52:55], v[34:37]
	v_pk_max_f16 v19, v1, 0
	v_mfma_f32_16x16x32_f16 v[20:23], v[30:33], v[56:59], v[20:23]
	s_nop 6
	v_cvt_pk_f16_f32 v0, v34, v35
	v_cvt_pk_f16_f32 v1, v36, v37
	v_pk_max_f16 v28, v0, 0
	v_pk_max_f16 v29, v1, 0
	v_cvt_pk_f16_f32 v0, v20, v21
	v_cvt_pk_f16_f32 v1, v22, v23
	v_pk_max_f16 v20, v0, 0
	v_pk_max_f16 v21, v1, 0
	v_mfma_f32_16x16x32_f16 v[24:27], v[44:47], v[26:29], 0
	s_nop 0
	v_mfma_f32_16x16x32_f16 v[18:21], v[44:47], v[18:21], 0
	s_nop 7
	v_cndmask_b32_e64 v18, v24, v18, s[0:1]
	s_cbranch_scc0 .LBB0_37
